# v023 + gMLP in-place norm loop with 4 row loads in flight per batch
# baseline (speedup 1.0000x reference)
.LBB0_350:
	v_add_u32_e32 v11, s40, v198
	ds_read2_b32 v[20:21], v10 offset1:4
	ds_read2_b32 v[22:23], v10 offset0:8 offset1:12
	ds_read2_b32 v[16:17], v10 offset0:16 offset1:20
	ds_read2_b32 v[226:227], v10 offset0:24 offset1:28
	v_add_u32_e32 v10, 0x80, v10
	s_add_i32 s40, s40, 32
	v_add_u32_e32 v12, 0xffffc000, v11
	v_ashrrev_i32_e32 v13, 31, v12
	v_lshlrev_b64 v[12:13], 12, v[12:13]
	v_lshl_add_u64 v[244:245], v[78:79], 0, v[12:13]
	global_load_dwordx4 v[228:231], v[244:245], off
	v_add_u32_e32 v12, 0xffffc004, v11
	v_ashrrev_i32_e32 v13, 31, v12
	v_lshlrev_b64 v[12:13], 12, v[12:13]
	v_lshl_add_u64 v[246:247], v[78:79], 0, v[12:13]
	global_load_dwordx4 v[232:235], v[246:247], off
	v_add_u32_e32 v12, 0xffffc008, v11
	v_ashrrev_i32_e32 v13, 31, v12
	v_lshlrev_b64 v[12:13], 12, v[12:13]
	v_lshl_add_u64 v[248:249], v[78:79], 0, v[12:13]
	global_load_dwordx4 v[236:239], v[248:249], off
	v_add_u32_e32 v12, 0xffffc00c, v11
	v_ashrrev_i32_e32 v13, 31, v12
	v_lshlrev_b64 v[12:13], 12, v[12:13]
	v_lshl_add_u64 v[250:251], v[78:79], 0, v[12:13]
	global_load_dwordx4 v[240:243], v[250:251], off
	s_waitcnt lgkmcnt(0)
	s_waitcnt vmcnt(3)
	v_mov_b32_e32 v14, v20
	v_lshlrev_b32_e32 v18, 16, v228
	v_and_b32_e32 v19, 0xffff0000, v228
	v_pk_mul_f32 v[18:19], v[14:15], v[18:19] op_sel_hi:[0,1]
	v_pk_mul_f32 v[18:19], v[6:7], v[18:19]
	s_nop 0
	v_cvt_pk_bf16_f32 v228, v18, v19
	v_lshlrev_b32_e32 v18, 16, v229
	v_and_b32_e32 v19, 0xffff0000, v229
	v_pk_mul_f32 v[18:19], v[14:15], v[18:19] op_sel_hi:[0,1]
	v_pk_mul_f32 v[18:19], v[8:9], v[18:19]
	s_nop 0
	v_cvt_pk_bf16_f32 v229, v18, v19
	v_lshlrev_b32_e32 v18, 16, v230
	v_and_b32_e32 v19, 0xffff0000, v230
	v_pk_mul_f32 v[18:19], v[14:15], v[18:19] op_sel_hi:[0,1]
	v_pk_mul_f32 v[18:19], v[2:3], v[18:19]
	s_nop 0
	v_cvt_pk_bf16_f32 v230, v18, v19
	v_lshlrev_b32_e32 v18, 16, v231
	v_and_b32_e32 v19, 0xffff0000, v231
	v_pk_mul_f32 v[18:19], v[14:15], v[18:19] op_sel_hi:[0,1]
	v_pk_mul_f32 v[18:19], v[4:5], v[18:19]
	s_nop 0
	v_cvt_pk_bf16_f32 v231, v18, v19
	global_store_dwordx4 v[244:245], v[228:231], off
	s_waitcnt vmcnt(3)
	v_mov_b32_e32 v14, v21
	v_lshlrev_b32_e32 v18, 16, v232
	v_and_b32_e32 v19, 0xffff0000, v232
	v_pk_mul_f32 v[18:19], v[14:15], v[18:19] op_sel_hi:[0,1]
	v_pk_mul_f32 v[18:19], v[6:7], v[18:19]
	s_nop 0
	v_cvt_pk_bf16_f32 v232, v18, v19
	v_lshlrev_b32_e32 v18, 16, v233
	v_and_b32_e32 v19, 0xffff0000, v233
	v_pk_mul_f32 v[18:19], v[14:15], v[18:19] op_sel_hi:[0,1]
	v_pk_mul_f32 v[18:19], v[8:9], v[18:19]
	s_nop 0
	v_cvt_pk_bf16_f32 v233, v18, v19
	v_lshlrev_b32_e32 v18, 16, v234
	v_and_b32_e32 v19, 0xffff0000, v234
	v_pk_mul_f32 v[18:19], v[14:15], v[18:19] op_sel_hi:[0,1]
	v_pk_mul_f32 v[18:19], v[2:3], v[18:19]
	s_nop 0
	v_cvt_pk_bf16_f32 v234, v18, v19
	v_lshlrev_b32_e32 v18, 16, v235
	v_and_b32_e32 v19, 0xffff0000, v235
	v_pk_mul_f32 v[18:19], v[14:15], v[18:19] op_sel_hi:[0,1]
	v_pk_mul_f32 v[18:19], v[4:5], v[18:19]
	s_nop 0
	v_cvt_pk_bf16_f32 v235, v18, v19
	global_store_dwordx4 v[246:247], v[232:235], off
	s_waitcnt vmcnt(3)
	v_mov_b32_e32 v14, v22
	v_lshlrev_b32_e32 v18, 16, v236
	v_and_b32_e32 v19, 0xffff0000, v236
	v_pk_mul_f32 v[18:19], v[14:15], v[18:19] op_sel_hi:[0,1]
	v_pk_mul_f32 v[18:19], v[6:7], v[18:19]
	s_nop 0
	v_cvt_pk_bf16_f32 v236, v18, v19
	v_lshlrev_b32_e32 v18, 16, v237
	v_and_b32_e32 v19, 0xffff0000, v237
	v_pk_mul_f32 v[18:19], v[14:15], v[18:19] op_sel_hi:[0,1]
	v_pk_mul_f32 v[18:19], v[8:9], v[18:19]
	s_nop 0
	v_cvt_pk_bf16_f32 v237, v18, v19
	v_lshlrev_b32_e32 v18, 16, v238
	v_and_b32_e32 v19, 0xffff0000, v238
	v_pk_mul_f32 v[18:19], v[14:15], v[18:19] op_sel_hi:[0,1]
	v_pk_mul_f32 v[18:19], v[2:3], v[18:19]
	s_nop 0
	v_cvt_pk_bf16_f32 v238, v18, v19
	v_lshlrev_b32_e32 v18, 16, v239
	v_and_b32_e32 v19, 0xffff0000, v239
	v_pk_mul_f32 v[18:19], v[14:15], v[18:19] op_sel_hi:[0,1]
	v_pk_mul_f32 v[18:19], v[4:5], v[18:19]
	s_nop 0
	v_cvt_pk_bf16_f32 v239, v18, v19
	global_store_dwordx4 v[248:249], v[236:239], off
	s_waitcnt vmcnt(3)
	v_mov_b32_e32 v14, v23
	v_lshlrev_b32_e32 v18, 16, v240
	v_and_b32_e32 v19, 0xffff0000, v240
	v_pk_mul_f32 v[18:19], v[14:15], v[18:19] op_sel_hi:[0,1]
	v_pk_mul_f32 v[18:19], v[6:7], v[18:19]
	s_nop 0
	v_cvt_pk_bf16_f32 v240, v18, v19
	v_lshlrev_b32_e32 v18, 16, v241
	v_and_b32_e32 v19, 0xffff0000, v241
	v_pk_mul_f32 v[18:19], v[14:15], v[18:19] op_sel_hi:[0,1]
	v_pk_mul_f32 v[18:19], v[8:9], v[18:19]
	s_nop 0
	v_cvt_pk_bf16_f32 v241, v18, v19
	v_lshlrev_b32_e32 v18, 16, v242
	v_and_b32_e32 v19, 0xffff0000, v242
	v_pk_mul_f32 v[18:19], v[14:15], v[18:19] op_sel_hi:[0,1]
	v_pk_mul_f32 v[18:19], v[2:3], v[18:19]
	s_nop 0
	v_cvt_pk_bf16_f32 v242, v18, v19
	v_lshlrev_b32_e32 v18, 16, v243
	v_and_b32_e32 v19, 0xffff0000, v243
	v_pk_mul_f32 v[18:19], v[14:15], v[18:19] op_sel_hi:[0,1]
	v_pk_mul_f32 v[18:19], v[4:5], v[18:19]
	s_nop 0
	v_cvt_pk_bf16_f32 v243, v18, v19
	global_store_dwordx4 v[250:251], v[240:243], off
	v_add_u32_e32 v12, 0xffffc010, v11
	v_ashrrev_i32_e32 v13, 31, v12
	v_lshlrev_b64 v[12:13], 12, v[12:13]
	v_lshl_add_u64 v[244:245], v[78:79], 0, v[12:13]
	global_load_dwordx4 v[228:231], v[244:245], off
	v_add_u32_e32 v12, 0xffffc014, v11
	v_ashrrev_i32_e32 v13, 31, v12
	v_lshlrev_b64 v[12:13], 12, v[12:13]
	v_lshl_add_u64 v[246:247], v[78:79], 0, v[12:13]
	global_load_dwordx4 v[232:235], v[246:247], off
	v_add_u32_e32 v12, 0xffffc018, v11
	v_ashrrev_i32_e32 v13, 31, v12
	v_lshlrev_b64 v[12:13], 12, v[12:13]
	v_lshl_add_u64 v[248:249], v[78:79], 0, v[12:13]
	global_load_dwordx4 v[236:239], v[248:249], off
	v_add_u32_e32 v12, 0xffffc01c, v11
	v_ashrrev_i32_e32 v13, 31, v12
	v_lshlrev_b64 v[12:13], 12, v[12:13]
	v_lshl_add_u64 v[250:251], v[78:79], 0, v[12:13]
	global_load_dwordx4 v[240:243], v[250:251], off
	s_waitcnt vmcnt(3)
	v_mov_b32_e32 v14, v16
	v_lshlrev_b32_e32 v18, 16, v228
	v_and_b32_e32 v19, 0xffff0000, v228
	v_pk_mul_f32 v[18:19], v[14:15], v[18:19] op_sel_hi:[0,1]
	v_pk_mul_f32 v[18:19], v[6:7], v[18:19]
	s_nop 0
	v_cvt_pk_bf16_f32 v228, v18, v19
	v_lshlrev_b32_e32 v18, 16, v229
	v_and_b32_e32 v19, 0xffff0000, v229
	v_pk_mul_f32 v[18:19], v[14:15], v[18:19] op_sel_hi:[0,1]
	v_pk_mul_f32 v[18:19], v[8:9], v[18:19]
	s_nop 0
	v_cvt_pk_bf16_f32 v229, v18, v19
	v_lshlrev_b32_e32 v18, 16, v230
	v_and_b32_e32 v19, 0xffff0000, v230
	v_pk_mul_f32 v[18:19], v[14:15], v[18:19] op_sel_hi:[0,1]
	v_pk_mul_f32 v[18:19], v[2:3], v[18:19]
	s_nop 0
	v_cvt_pk_bf16_f32 v230, v18, v19
	v_lshlrev_b32_e32 v18, 16, v231
	v_and_b32_e32 v19, 0xffff0000, v231
	v_pk_mul_f32 v[18:19], v[14:15], v[18:19] op_sel_hi:[0,1]
	v_pk_mul_f32 v[18:19], v[4:5], v[18:19]
	s_nop 0
	v_cvt_pk_bf16_f32 v231, v18, v19
	global_store_dwordx4 v[244:245], v[228:231], off
	s_waitcnt vmcnt(3)
	v_mov_b32_e32 v14, v17
	v_lshlrev_b32_e32 v18, 16, v232
	v_and_b32_e32 v19, 0xffff0000, v232
	v_pk_mul_f32 v[18:19], v[14:15], v[18:19] op_sel_hi:[0,1]
	v_pk_mul_f32 v[18:19], v[6:7], v[18:19]
	s_nop 0
	v_cvt_pk_bf16_f32 v232, v18, v19
	v_lshlrev_b32_e32 v18, 16, v233
	v_and_b32_e32 v19, 0xffff0000, v233
	v_pk_mul_f32 v[18:19], v[14:15], v[18:19] op_sel_hi:[0,1]
	v_pk_mul_f32 v[18:19], v[8:9], v[18:19]
	s_nop 0
	v_cvt_pk_bf16_f32 v233, v18, v19
	v_lshlrev_b32_e32 v18, 16, v234
	v_and_b32_e32 v19, 0xffff0000, v234
	v_pk_mul_f32 v[18:19], v[14:15], v[18:19] op_sel_hi:[0,1]
	v_pk_mul_f32 v[18:19], v[2:3], v[18:19]
	s_nop 0
	v_cvt_pk_bf16_f32 v234, v18, v19
	v_lshlrev_b32_e32 v18, 16, v235
	v_and_b32_e32 v19, 0xffff0000, v235
	v_pk_mul_f32 v[18:19], v[14:15], v[18:19] op_sel_hi:[0,1]
	v_pk_mul_f32 v[18:19], v[4:5], v[18:19]
	s_nop 0
	v_cvt_pk_bf16_f32 v235, v18, v19
	global_store_dwordx4 v[246:247], v[232:235], off
	s_waitcnt vmcnt(3)
	v_mov_b32_e32 v14, v226
	v_lshlrev_b32_e32 v18, 16, v236
	v_and_b32_e32 v19, 0xffff0000, v236
	v_pk_mul_f32 v[18:19], v[14:15], v[18:19] op_sel_hi:[0,1]
	v_pk_mul_f32 v[18:19], v[6:7], v[18:19]
	s_nop 0
	v_cvt_pk_bf16_f32 v236, v18, v19
	v_lshlrev_b32_e32 v18, 16, v237
	v_and_b32_e32 v19, 0xffff0000, v237
	v_pk_mul_f32 v[18:19], v[14:15], v[18:19] op_sel_hi:[0,1]
	v_pk_mul_f32 v[18:19], v[8:9], v[18:19]
	s_nop 0
	v_cvt_pk_bf16_f32 v237, v18, v19
	v_lshlrev_b32_e32 v18, 16, v238
	v_and_b32_e32 v19, 0xffff0000, v238
	v_pk_mul_f32 v[18:19], v[14:15], v[18:19] op_sel_hi:[0,1]
	v_pk_mul_f32 v[18:19], v[2:3], v[18:19]
	s_nop 0
	v_cvt_pk_bf16_f32 v238, v18, v19
	v_lshlrev_b32_e32 v18, 16, v239
	v_and_b32_e32 v19, 0xffff0000, v239
	v_pk_mul_f32 v[18:19], v[14:15], v[18:19] op_sel_hi:[0,1]
	v_pk_mul_f32 v[18:19], v[4:5], v[18:19]
	s_nop 0
	v_cvt_pk_bf16_f32 v239, v18, v19
	global_store_dwordx4 v[248:249], v[236:239], off
	s_waitcnt vmcnt(3)
	v_mov_b32_e32 v14, v227
	v_lshlrev_b32_e32 v18, 16, v240
	v_and_b32_e32 v19, 0xffff0000, v240
	v_pk_mul_f32 v[18:19], v[14:15], v[18:19] op_sel_hi:[0,1]
	v_pk_mul_f32 v[18:19], v[6:7], v[18:19]
	s_nop 0
	v_cvt_pk_bf16_f32 v240, v18, v19
	v_lshlrev_b32_e32 v18, 16, v241
	v_and_b32_e32 v19, 0xffff0000, v241
	v_pk_mul_f32 v[18:19], v[14:15], v[18:19] op_sel_hi:[0,1]
	v_pk_mul_f32 v[18:19], v[8:9], v[18:19]
	s_nop 0
	v_cvt_pk_bf16_f32 v241, v18, v19
	v_lshlrev_b32_e32 v18, 16, v242
	v_and_b32_e32 v19, 0xffff0000, v242
	v_pk_mul_f32 v[18:19], v[14:15], v[18:19] op_sel_hi:[0,1]
	v_pk_mul_f32 v[18:19], v[2:3], v[18:19]
	s_nop 0
	v_cvt_pk_bf16_f32 v242, v18, v19
	v_lshlrev_b32_e32 v18, 16, v243
	v_and_b32_e32 v19, 0xffff0000, v243
	v_pk_mul_f32 v[18:19], v[14:15], v[18:19] op_sel_hi:[0,1]
	v_pk_mul_f32 v[18:19], v[4:5], v[18:19]
	s_nop 0
	v_cvt_pk_bf16_f32 v243, v18, v19
	global_store_dwordx4 v[250:251], v[240:243], off
	s_cmpk_lg_i32 s40, 0x80
	s_cbranch_scc1 .LBB0_350
	s_mov_b64 s[40:41], 0
	s_barrier
